# router phase tail: four bias loads issued together with counted waits; the exec-masked bias word loaded once instead of four load/wait round trips
# baseline (speedup 1.0000x reference)
; #define RT_WLOAD(W, c) do { const int cw_ = (c) < 16 ? (c) : 15; _Pragma("unroll") for (int i = 0; i < 3; ++i) { RT_TASK(i); W[i] = *(const GAS v4u*)(RW + (size_t)row * DM + cw_ * 128 + seg * 8); } } while (0)
; #define RT_WSTORE(W, c) do { _Pragma("unroll") for (int i = 0; i < 3; ++i) { RT_TASK(i); *(LAS v4u*)(wb + ((c) & 1) * WBUF + row * WROW + seg * 8) = W[i]; } } while (0)
; #define RT_XLOAD(XB, c) do { const int cc_ = (c) < 16 ? (c) : 15; _Pragma("unroll") for (int ks = 0; ks < 4; ++ks) XB[ks] = *(const GAS v4u*)(xrow + cc_ * 128 + 32 * ks); } while (0)
; #define RT_CHUNK(c, XB) do { const LAS bf16* cur = wb + ((c) & 1) * WBUF + c16 * WROW + 8 * g4; bf16x8 hA[5], hB[5]; RT_HLOAD(hA, 0); \
;         RT_HLOAD(hB, 1); RT_KSTEP(c, XB, 0, hA); RT_HLOAD(hA, 2); RT_KSTEP(c, XB, 1, hB); RT_HLOAD(hB, 3); RT_KSTEP(c, XB, 2, hA); RT_KSTEP(c, XB, 3, hB); } while (0)
; __device__ __forceinline__ void router_phase(const Ctx& C, const bf16* X, const float* rowss, const bf16* RW, const float* gain, const float* bg, const float* be, unsigned char* XN8, unsigned char* rt) {
;     ...
;     RT_WLOAD(wA, 0); RT_XLOAD(x0, 0); RT_XLOAD(x1, 1); RT_XLOAD(x2, 2); RT_WLOAD(wB, 1); RT_WSTORE(wA, 0);
;     __syncthreads();
; #pragma unroll 1
;     for (int c = 0; c < 16; c += 4) {
;         RT_WLOAD(wA, c + 2); RT_XLOAD(x3, c + 3); RT_CHUNK(c, x0); RT_WSTORE(wB, c + 1); __syncthreads();
;         RT_WLOAD(wB, c + 3); RT_XLOAD(x0, c + 4); RT_CHUNK(c + 1, x1); RT_WSTORE(wA, c + 2); __syncthreads();
;         RT_WLOAD(wA, c + 4); RT_XLOAD(x1, c + 5); RT_CHUNK(c + 2, x2); RT_WSTORE(wB, c + 3); __syncthreads();
;         RT_WLOAD(wB, c + 5); RT_XLOAD(x2, c + 6); RT_CHUNK(c + 3, x3); RT_WSTORE(wA, c + 4); __syncthreads();
.LBB0_986:
	v_lshl_add_u64 v[64:65], s[0:1], 0, v[168:169]
	v_add_co_u32_e32 v112, vcc, s22, v64
	s_add_i32 s17, s9, 4
	s_nop 0
	v_addc_co_u32_e32 v113, vcc, 0, v65, vcc
	v_lshl_add_u64 v[64:65], s[0:1], 0, v[166:167]
	v_add_co_u32_e32 v114, vcc, s22, v64
	global_load_dwordx4 v[100:103], v[112:113], off offset:512
	s_nop 0
	v_addc_co_u32_e32 v115, vcc, 0, v65, vcc
	v_lshl_add_u64 v[64:65], s[0:1], 0, v[164:165]
	v_add_co_u32_e32 v116, vcc, s22, v64
	global_load_dwordx4 v[104:107], v[114:115], off offset:512
	s_nop 0
	v_addc_co_u32_e32 v117, vcc, 0, v65, vcc
	v_lshl_add_u64 v[64:65], s[0:1], 0, v[162:163]
	v_add_co_u32_e32 v64, vcc, s23, v64
	global_load_dwordx4 v[108:111], v[116:117], off offset:512
	s_nop 0
	v_addc_co_u32_e32 v65, vcc, 0, v65, vcc
	global_load_dwordx4 v[76:79], v[64:65], off offset:768
	global_load_dwordx4 v[72:75], v[64:65], off offset:832
	global_load_dwordx4 v[68:71], v[64:65], off offset:896
	s_nop 0
	global_load_dwordx4 v[64:67], v[64:65], off offset:960
	ds_read_b128 v[118:121], v184 offset:24576
	ds_read_b128 v[122:125], v184 offset:28928
	ds_read_b128 v[126:129], v184 offset:33280
	ds_read_b128 v[130:133], v184 offset:37632
	ds_read_b128 v[134:137], v184 offset:41984
	ds_read_b128 v[138:141], v184 offset:24640
	ds_read_b128 v[142:145], v184 offset:28992
	ds_read_b128 v[146:149], v184 offset:33344
	ds_read_b128 v[190:193], v184 offset:37696
	ds_read_b128 v[194:197], v184 offset:42048
	s_waitcnt vmcnt(8) lgkmcnt(9)
	v_mfma_f32_16x16x32_bf16 v[80:83], v[44:47], v[118:121], v[80:83]
	s_cmp_lt_u32 s9, 12
	s_cselect_b32 s30, s16, 0x780
	s_lshl_b64 s[18:19], s[30:31], 1
	s_waitcnt lgkmcnt(8)
	v_mfma_f32_16x16x32_bf16 v[92:95], v[44:47], v[122:125], v[92:95]
	ds_read_b128 v[118:121], v189
	ds_read_b128 v[122:125], v189 offset:16
	s_add_u32 s12, s2, s18
	s_addc_u32 s13, s3, s19
	s_waitcnt lgkmcnt(9)
	v_mfma_f32_16x16x32_bf16 v[88:91], v[44:47], v[126:129], v[88:91]
	v_lshlrev_b32_e32 v126, 16, v44
	v_mul_f32_e32 v126, v180, v126
	s_waitcnt lgkmcnt(1)
	v_mul_f32_e32 v118, v126, v118
	v_mfma_f32_16x16x32_bf16 v[96:99], v[44:47], v[130:133], v[96:99]
	v_med3_f32 v118, v118, s33, v214
	v_mov_b32_e32 v171, v2
	v_mov_b32_e32 v173, v2
	v_mfma_f32_16x16x32_bf16 v[84:87], v[44:47], v[134:137], v[84:87]
	v_and_b32_e32 v44, 0xffff0000, v44
	v_mul_f32_e32 v44, v180, v44
	v_mul_f32_e32 v44, v44, v119
	v_lshlrev_b32_e32 v119, 16, v45
	v_mul_f32_e32 v119, v180, v119
	v_mul_f32_e32 v119, v119, v120
	v_med3_f32 v120, v44, s33, v214
	v_mov_b32_e32 v44, v2
	v_and_b32_e32 v45, 0xffff0000, v45
	v_cvt_pk_fp8_f32 v44, v118, v120
	v_mul_f32_e32 v45, v180, v45
	v_mul_f32_e32 v45, v45, v121
	v_med3_f32 v119, v119, s33, v214
	v_med3_f32 v45, v45, s33, v214
	v_cvt_pk_fp8_f32 v44, v119, v45 op_sel:[0,0,1]
	v_lshlrev_b32_e32 v45, 16, v46
	v_and_b32_e32 v46, 0xffff0000, v46
	v_mul_f32_e32 v45, v180, v45
	v_mul_f32_e32 v46, v180, v46
	s_waitcnt lgkmcnt(0)
	v_mul_f32_e32 v45, v45, v122
	v_mul_f32_e32 v46, v46, v123
	v_med3_f32 v119, v45, s33, v214
	v_med3_f32 v46, v46, s33, v214
	v_mov_b32_e32 v45, v2
	v_lshlrev_b32_e32 v118, 16, v47
	v_and_b32_e32 v47, 0xffff0000, v47
	v_cvt_pk_fp8_f32 v45, v119, v46
	v_mul_f32_e32 v118, v180, v118
	v_mul_f32_e32 v47, v180, v47
	v_mul_f32_e32 v118, v118, v124
	v_mul_f32_e32 v47, v47, v125
	v_med3_f32 v118, v118, s33, v214
	v_med3_f32 v47, v47, s33, v214
	v_cvt_pk_fp8_f32 v45, v118, v47 op_sel:[0,0,1]
	v_lshl_add_u64 v[46:47], s[0:1], 0, v[160:161]
	v_add_co_u32_e32 v174, vcc, s24, v46
	v_mfma_f32_16x16x32_bf16 v[80:83], v[32:35], v[138:141], v[80:83]
	s_nop 0
	v_addc_co_u32_e32 v175, vcc, 0, v47, vcc
	global_store_dwordx2 v[174:175], v[44:45], off
	ds_read_b128 v[44:47], v184 offset:24704
	ds_read_b128 v[118:121], v184 offset:29056
	ds_read_b128 v[122:125], v184 offset:33408
	ds_read_b128 v[126:129], v184 offset:37760
	ds_read_b128 v[130:133], v184 offset:42112
	ds_read_b128 v[134:137], v189 offset:128
	ds_read_b128 v[138:141], v189 offset:144
	v_mfma_f32_16x16x32_bf16 v[92:95], v[32:35], v[142:145], v[92:95]
	v_lshlrev_b32_e32 v142, 16, v32
	v_mul_f32_e32 v142, v180, v142
	s_waitcnt lgkmcnt(1)
	v_mul_f32_e32 v134, v142, v134
	v_mfma_f32_16x16x32_bf16 v[88:91], v[32:35], v[146:149], v[88:91]
	v_med3_f32 v134, v134, s33, v214
	s_min_u32 s8, s9, 10
	s_lshl_b32 s30, s8, 8
	v_mfma_f32_16x16x32_bf16 v[96:99], v[32:35], v[190:193], v[96:99]
	s_add_u32 s10, s2, s30
	s_addc_u32 s11, s3, 0
	s_min_u32 s8, s9, 9
	v_mfma_f32_16x16x32_bf16 v[84:87], v[32:35], v[194:197], v[84:87]
	v_and_b32_e32 v32, 0xffff0000, v32
	v_mul_f32_e32 v32, v180, v32
	v_mul_f32_e32 v32, v32, v135
	v_lshlrev_b32_e32 v135, 16, v33
	v_mul_f32_e32 v135, v180, v135
	v_mul_f32_e32 v135, v135, v136
	v_med3_f32 v136, v32, s33, v214
	v_mov_b32_e32 v32, v2
	v_and_b32_e32 v33, 0xffff0000, v33
	v_cvt_pk_fp8_f32 v32, v134, v136
	v_mul_f32_e32 v33, v180, v33
	v_mul_f32_e32 v33, v33, v137
	v_med3_f32 v135, v135, s33, v214
	v_med3_f32 v33, v33, s33, v214
	v_cvt_pk_fp8_f32 v32, v135, v33 op_sel:[0,0,1]
	v_lshlrev_b32_e32 v33, 16, v34
	v_and_b32_e32 v34, 0xffff0000, v34
	v_mul_f32_e32 v33, v180, v33
	v_mul_f32_e32 v34, v180, v34
	s_waitcnt lgkmcnt(0)
; #define RT_WLOAD(W, c) do { const int cw_ = (c) < 16 ? (c) : 15; _Pragma("unroll") for (int i = 0; i < 3; ++i) { RT_TASK(i); W[i] = *(const GAS v4u*)(RW + (size_t)row * DM + cw_ * 128 + seg * 8); } } while (0)
; #define RT_WSTORE(W, c) do { _Pragma("unroll") for (int i = 0; i < 3; ++i) { RT_TASK(i); *(LAS v4u*)(wb + ((c) & 1) * WBUF + row * WROW + seg * 8) = W[i]; } } while (0)
; #define RT_XLOAD(XB, c) do { const int cc_ = (c) < 16 ? (c) : 15; _Pragma("unroll") for (int ks = 0; ks < 4; ++ks) XB[ks] = *(const GAS v4u*)(xrow + cc_ * 128 + 32 * ks); } while (0)
; #define RT_CHUNK(c, XB) do { const LAS bf16* cur = wb + ((c) & 1) * WBUF + c16 * WROW + 8 * g4; bf16x8 hA[5], hB[5]; RT_HLOAD(hA, 0); \
;         RT_HLOAD(hB, 1); RT_KSTEP(c, XB, 0, hA); RT_HLOAD(hA, 2); RT_KSTEP(c, XB, 1, hB); RT_HLOAD(hB, 3); RT_KSTEP(c, XB, 2, hA); RT_KSTEP(c, XB, 3, hB); } while (0)
; __device__ __forceinline__ void router_phase(const Ctx& C, const bf16* X, const float* rowss, const bf16* RW, const float* gain, const float* bg, const float* be, unsigned char* XN8, unsigned char* rt) {
;     ...
;     RT_WLOAD(wA, 0); RT_XLOAD(x0, 0); RT_XLOAD(x1, 1); RT_XLOAD(x2, 2); RT_WLOAD(wB, 1); RT_WSTORE(wA, 0);
;     __syncthreads();
; #pragma unroll 1
;     for (int c = 0; c < 16; c += 4) {
;         RT_WLOAD(wA, c + 2); RT_XLOAD(x3, c + 3); RT_CHUNK(c, x0); RT_WSTORE(wB, c + 1); __syncthreads();
;         RT_WLOAD(wB, c + 3); RT_XLOAD(x0, c + 4); RT_CHUNK(c + 1, x1); RT_WSTORE(wA, c + 2); __syncthreads();
;         RT_WLOAD(wA, c + 4); RT_XLOAD(x1, c + 5); RT_CHUNK(c + 2, x2); RT_WSTORE(wB, c + 3); __syncthreads();
;         RT_WLOAD(wB, c + 5); RT_XLOAD(x2, c + 6); RT_CHUNK(c + 3, x3); RT_WSTORE(wA, c + 4); __syncthreads();
	v_mul_f32_e32 v33, v33, v138
	v_mul_f32_e32 v34, v34, v139
	v_med3_f32 v135, v33, s33, v214
	v_med3_f32 v34, v34, s33, v214
	v_mov_b32_e32 v33, v2
	v_lshlrev_b32_e32 v134, 16, v35
	v_and_b32_e32 v35, 0xffff0000, v35
	v_cvt_pk_fp8_f32 v33, v135, v34
	v_mul_f32_e32 v134, v180, v134
	v_mul_f32_e32 v35, v180, v35
	v_mul_f32_e32 v134, v134, v140
	v_mul_f32_e32 v35, v35, v141
	v_med3_f32 v134, v134, s33, v214
	v_med3_f32 v35, v35, s33, v214
	v_cvt_pk_fp8_f32 v33, v134, v35 op_sel:[0,0,1]
	v_mfma_f32_16x16x32_bf16 v[44:47], v[24:27], v[44:47], v[80:83]
	s_lshl_b32 s8, s8, 8
	s_addk_i32 s16, 0x200
	global_store_dwordx2 v[174:175], v[32:33], off offset:32
	ds_read_b128 v[32:35], v184 offset:24768
	ds_read_b128 v[134:137], v184 offset:29120
	ds_read_b128 v[138:141], v184 offset:33472
	ds_read_b128 v[142:145], v184 offset:37824
	ds_read_b128 v[146:149], v184 offset:42176
	v_mfma_f32_16x16x32_bf16 v[92:95], v[24:27], v[118:121], v[92:95]
	s_cmp_gt_u32 s9, 11
	s_mov_b32 s9, s31
	v_lshl_add_u64 v[162:163], v[162:163], 0, s[26:27]
	v_mfma_f32_16x16x32_bf16 v[118:121], v[24:27], v[130:133], v[84:87]
	ds_read_b128 v[80:83], v189 offset:256
	s_nop 1
	ds_read_b128 v[84:87], v189 offset:272
	v_lshl_add_u64 v[164:165], v[164:165], 0, s[26:27]
	v_lshl_add_u64 v[166:167], v[166:167], 0, s[26:27]
	v_mfma_f32_16x16x32_bf16 v[88:91], v[24:27], v[122:125], v[88:91]
	v_lshlrev_b32_e32 v122, 16, v24
	v_mul_f32_e32 v122, v180, v122
	s_waitcnt lgkmcnt(1)
	v_mul_f32_e32 v80, v122, v80
	v_mfma_f32_16x16x32_bf16 v[96:99], v[24:27], v[126:129], v[96:99]
	v_and_b32_e32 v24, 0xffff0000, v24
	v_mul_f32_e32 v24, v180, v24
	v_mul_f32_e32 v24, v24, v81
	v_lshlrev_b32_e32 v81, 16, v25
	v_mul_f32_e32 v81, v180, v81
	v_mul_f32_e32 v81, v81, v82
	v_med3_f32 v80, v80, s33, v214
	v_med3_f32 v82, v24, s33, v214
	v_mov_b32_e32 v24, v2
	v_and_b32_e32 v25, 0xffff0000, v25
	v_cvt_pk_fp8_f32 v24, v80, v82
	v_mul_f32_e32 v25, v180, v25
	v_mul_f32_e32 v25, v25, v83
	v_med3_f32 v81, v81, s33, v214
	v_med3_f32 v25, v25, s33, v214
	v_cvt_pk_fp8_f32 v24, v81, v25 op_sel:[0,0,1]
	v_lshlrev_b32_e32 v25, 16, v26
	v_and_b32_e32 v26, 0xffff0000, v26
	v_mul_f32_e32 v25, v180, v25
	v_mul_f32_e32 v26, v180, v26
	s_waitcnt lgkmcnt(0)
	v_mul_f32_e32 v25, v25, v84
	v_mul_f32_e32 v26, v26, v85
	v_med3_f32 v81, v25, s33, v214
	v_med3_f32 v26, v26, s33, v214
	v_mov_b32_e32 v25, v2
	v_lshlrev_b32_e32 v80, 16, v27
	v_and_b32_e32 v27, 0xffff0000, v27
	v_cvt_pk_fp8_f32 v25, v81, v26
	v_mul_f32_e32 v80, v180, v80
	v_mul_f32_e32 v27, v180, v27
	v_mul_f32_e32 v80, v80, v86
	v_mul_f32_e32 v27, v27, v87
	v_med3_f32 v80, v80, s33, v214
	v_med3_f32 v27, v27, s33, v214
	v_cvt_pk_fp8_f32 v25, v80, v27 op_sel:[0,0,1]
	v_mfma_f32_16x16x32_bf16 v[80:83], v[12:15], v[32:35], v[44:47]
	v_lshl_add_u64 v[168:169], v[168:169], 0, s[26:27]
	global_store_dwordx2 v[174:175], v[24:25], off offset:64
	ds_read_b128 v[24:27], v189 offset:384
	ds_read_b128 v[32:35], v189 offset:400
	v_mfma_f32_16x16x32_bf16 v[84:87], v[12:15], v[134:137], v[92:95]
	v_lshlrev_b32_e32 v44, 16, v12
	v_mul_f32_e32 v44, v180, v44
	s_waitcnt lgkmcnt(1)
	v_mul_f32_e32 v24, v44, v24
	v_mfma_f32_16x16x32_bf16 v[88:91], v[12:15], v[138:141], v[88:91]
	v_med3_f32 v24, v24, s33, v214
	v_mfma_f32_16x16x32_bf16 v[92:95], v[12:15], v[142:145], v[96:99]
	v_mfma_f32_16x16x32_bf16 v[96:99], v[12:15], v[146:149], v[118:121]
	v_and_b32_e32 v12, 0xffff0000, v12
	v_mul_f32_e32 v12, v180, v12
	v_mul_f32_e32 v12, v12, v25
	v_lshlrev_b32_e32 v25, 16, v13
	v_mul_f32_e32 v25, v180, v25
	v_mul_f32_e32 v25, v25, v26
	v_med3_f32 v26, v12, s33, v214
	v_mov_b32_e32 v12, v2
	v_and_b32_e32 v13, 0xffff0000, v13
	v_cvt_pk_fp8_f32 v12, v24, v26
	v_mul_f32_e32 v13, v180, v13
	v_mul_f32_e32 v13, v13, v27
	v_med3_f32 v25, v25, s33, v214
	v_med3_f32 v13, v13, s33, v214
	v_cvt_pk_fp8_f32 v12, v25, v13 op_sel:[0,0,1]
	v_lshlrev_b32_e32 v13, 16, v14
	v_and_b32_e32 v14, 0xffff0000, v14
	v_mul_f32_e32 v13, v180, v13
	v_mul_f32_e32 v14, v180, v14
	s_waitcnt lgkmcnt(0)
	v_mul_f32_e32 v13, v13, v32
	v_mul_f32_e32 v14, v14, v33
	v_med3_f32 v25, v13, s33, v214
	v_med3_f32 v14, v14, s33, v214
	v_mov_b32_e32 v13, v2
	v_lshlrev_b32_e32 v24, 16, v15
	v_and_b32_e32 v15, 0xffff0000, v15
	v_cvt_pk_fp8_f32 v13, v25, v14
	v_mul_f32_e32 v24, v180, v24
	v_mul_f32_e32 v15, v180, v15
	v_mul_f32_e32 v24, v24, v34
	v_mul_f32_e32 v15, v15, v35
	v_med3_f32 v24, v24, s33, v214
	v_med3_f32 v15, v15, s33, v214
	v_cvt_pk_fp8_f32 v13, v24, v15 op_sel:[0,0,1]
	global_store_dwordx2 v[174:175], v[12:13], off offset:96
	v_lshl_add_u64 v[12:13], v[158:159], 0, s[18:19]
	ds_write_b128 v186, v[60:63]
	ds_write_b128 v187, v[56:59]
	s_waitcnt vmcnt(11)
	ds_write_b128 v188, v[52:55]
	s_waitcnt lgkmcnt(0)
	s_barrier
; #define RT_WLOAD(W, c) do { const int cw_ = (c) < 16 ? (c) : 15; _Pragma("unroll") for (int i = 0; i < 3; ++i) { RT_TASK(i); W[i] = *(const GAS v4u*)(RW + (size_t)row * DM + cw_ * 128 + seg * 8); } } while (0)
; #define RT_WSTORE(W, c) do { _Pragma("unroll") for (int i = 0; i < 3; ++i) { RT_TASK(i); *(LAS v4u*)(wb + ((c) & 1) * WBUF + row * WROW + seg * 8) = W[i]; } } while (0)
; #define RT_XLOAD(XB, c) do { const int cc_ = (c) < 16 ? (c) : 15; _Pragma("unroll") for (int ks = 0; ks < 4; ++ks) XB[ks] = *(const GAS v4u*)(xrow + cc_ * 128 + 32 * ks); } while (0)
; #define RT_CHUNK(c, XB) do { const LAS bf16* cur = wb + ((c) & 1) * WBUF + c16 * WROW + 8 * g4; bf16x8 hA[5], hB[5]; RT_HLOAD(hA, 0); \
;         RT_HLOAD(hB, 1); RT_KSTEP(c, XB, 0, hA); RT_HLOAD(hA, 2); RT_KSTEP(c, XB, 1, hB); RT_HLOAD(hB, 3); RT_KSTEP(c, XB, 2, hA); RT_KSTEP(c, XB, 3, hB); } while (0)
; __device__ __forceinline__ void router_phase(const Ctx& C, const bf16* X, const float* rowss, const bf16* RW, const float* gain, const float* bg, const float* be, unsigned char* XN8, unsigned char* rt) {
;     ...
;     RT_WLOAD(wA, 0); RT_XLOAD(x0, 0); RT_XLOAD(x1, 1); RT_XLOAD(x2, 2); RT_WLOAD(wB, 1); RT_WSTORE(wA, 0);
;     __syncthreads();
; #pragma unroll 1
;     for (int c = 0; c < 16; c += 4) {
;         RT_WLOAD(wA, c + 2); RT_XLOAD(x3, c + 3); RT_CHUNK(c, x0); RT_WSTORE(wB, c + 1); __syncthreads();
;         RT_WLOAD(wB, c + 3); RT_XLOAD(x0, c + 4); RT_CHUNK(c + 1, x1); RT_WSTORE(wA, c + 2); __syncthreads();
;         RT_WLOAD(wA, c + 4); RT_XLOAD(x1, c + 5); RT_CHUNK(c + 2, x2); RT_WSTORE(wB, c + 3); __syncthreads();
;         RT_WLOAD(wB, c + 5); RT_XLOAD(x2, c + 6); RT_CHUNK(c + 3, x3); RT_WSTORE(wA, c + 4); __syncthreads();
	global_load_dwordx4 v[52:55], v[112:113], off offset:768
	global_load_dwordx4 v[56:59], v[114:115], off offset:768
	global_load_dwordx4 v[60:63], v[116:117], off offset:768
	global_load_dwordx4 v[44:47], v[12:13], off
	global_load_dwordx4 v[32:35], v[12:13], off offset:64
	global_load_dwordx4 v[24:27], v[12:13], off offset:128
	s_nop 0
	global_load_dwordx4 v[12:15], v[12:13], off offset:192
	ds_read_b128 v[132:135], v185
	ds_read_b128 v[136:139], v185 offset:4352
	ds_read_b128 v[140:143], v185 offset:8704
	ds_read_b128 v[144:147], v185 offset:13056
	ds_read_b128 v[148:151], v185 offset:17408
	ds_read_b128 v[112:115], v185 offset:64
	ds_read_b128 v[116:119], v185 offset:4416
	ds_read_b128 v[120:123], v185 offset:8768
	ds_read_b128 v[124:127], v185 offset:13120
	ds_read_b128 v[128:131], v185 offset:17472
	s_waitcnt lgkmcnt(9)
	v_mfma_f32_16x16x32_bf16 v[80:83], v[40:43], v[132:135], v[80:83]
	s_waitcnt lgkmcnt(8)
	v_mfma_f32_16x16x32_bf16 v[84:87], v[40:43], v[136:139], v[84:87]
	ds_read_b128 v[136:139], v189 offset:512
	ds_read_b128 v[132:135], v189 offset:528
	s_waitcnt lgkmcnt(9)
	v_mfma_f32_16x16x32_bf16 v[88:91], v[40:43], v[140:143], v[88:91]
	v_lshlrev_b32_e32 v140, 16, v40
	v_mul_f32_e32 v140, v180, v140
	s_waitcnt lgkmcnt(1)
	v_mul_f32_e32 v136, v140, v136
	v_mfma_f32_16x16x32_bf16 v[92:95], v[40:43], v[144:147], v[92:95]
	v_med3_f32 v136, v136, s33, v214
	v_mfma_f32_16x16x32_bf16 v[96:99], v[40:43], v[148:151], v[96:99]
	v_and_b32_e32 v40, 0xffff0000, v40
	v_mul_f32_e32 v40, v180, v40
	v_mul_f32_e32 v40, v40, v137
	v_lshlrev_b32_e32 v137, 16, v41
	v_mul_f32_e32 v137, v180, v137
	v_mul_f32_e32 v137, v137, v138
	v_med3_f32 v138, v40, s33, v214
	v_mov_b32_e32 v40, v2
	v_and_b32_e32 v41, 0xffff0000, v41
	v_cvt_pk_fp8_f32 v40, v136, v138
	v_mul_f32_e32 v41, v180, v41
	v_mul_f32_e32 v41, v41, v139
	v_med3_f32 v137, v137, s33, v214
	v_med3_f32 v41, v41, s33, v214
	v_cvt_pk_fp8_f32 v40, v137, v41 op_sel:[0,0,1]
	v_lshlrev_b32_e32 v41, 16, v42
	v_and_b32_e32 v42, 0xffff0000, v42
	v_mul_f32_e32 v41, v180, v41
	v_mul_f32_e32 v42, v180, v42
	s_waitcnt lgkmcnt(0)
	v_mul_f32_e32 v41, v41, v132
	v_mul_f32_e32 v42, v42, v133
	v_med3_f32 v133, v41, s33, v214
	v_med3_f32 v42, v42, s33, v214
	v_mov_b32_e32 v41, v2
	v_lshlrev_b32_e32 v132, 16, v43
	v_and_b32_e32 v43, 0xffff0000, v43
	v_cvt_pk_fp8_f32 v41, v133, v42
	v_mul_f32_e32 v132, v180, v132
	v_mul_f32_e32 v43, v180, v43
	v_mul_f32_e32 v132, v132, v134
	v_mul_f32_e32 v43, v43, v135
	v_med3_f32 v132, v132, s33, v214
	v_med3_f32 v43, v43, s33, v214
	v_cvt_pk_fp8_f32 v41, v132, v43 op_sel:[0,0,1]
	v_mfma_f32_16x16x32_bf16 v[80:83], v[28:31], v[112:115], v[80:83]
	global_store_dwordx2 v[174:175], v[40:41], off offset:128
	ds_read_b128 v[40:43], v185 offset:128
	ds_read_b128 v[132:135], v185 offset:4480
	ds_read_b128 v[136:139], v185 offset:8832
	ds_read_b128 v[140:143], v185 offset:13184
	ds_read_b128 v[144:147], v185 offset:17536
	v_mfma_f32_16x16x32_bf16 v[84:87], v[28:31], v[116:119], v[84:87]
	ds_read_b128 v[112:115], v189 offset:640
	ds_read_b128 v[116:119], v189 offset:656
	v_mfma_f32_16x16x32_bf16 v[88:91], v[28:31], v[120:123], v[88:91]
	v_lshlrev_b32_e32 v120, 16, v28
	v_mul_f32_e32 v120, v180, v120
	s_waitcnt lgkmcnt(1)
	v_mul_f32_e32 v112, v120, v112
	v_mfma_f32_16x16x32_bf16 v[92:95], v[28:31], v[124:127], v[92:95]
	v_med3_f32 v112, v112, s33, v214
	v_mfma_f32_16x16x32_bf16 v[96:99], v[28:31], v[128:131], v[96:99]
	v_and_b32_e32 v28, 0xffff0000, v28
	v_mul_f32_e32 v28, v180, v28
	v_mul_f32_e32 v28, v28, v113
	v_lshlrev_b32_e32 v113, 16, v29
	v_mul_f32_e32 v113, v180, v113
	v_mul_f32_e32 v113, v113, v114
	v_med3_f32 v114, v28, s33, v214
	v_mov_b32_e32 v28, v2
	v_and_b32_e32 v29, 0xffff0000, v29
	v_cvt_pk_fp8_f32 v28, v112, v114
	v_mul_f32_e32 v29, v180, v29
	v_mul_f32_e32 v29, v29, v115
	v_med3_f32 v113, v113, s33, v214
	v_med3_f32 v29, v29, s33, v214
	v_cvt_pk_fp8_f32 v28, v113, v29 op_sel:[0,0,1]
	v_lshlrev_b32_e32 v29, 16, v30
	v_and_b32_e32 v30, 0xffff0000, v30
	v_mul_f32_e32 v29, v180, v29
	v_mul_f32_e32 v30, v180, v30
	s_waitcnt lgkmcnt(0)
	v_mul_f32_e32 v29, v29, v116
	v_mul_f32_e32 v30, v30, v117
	v_med3_f32 v113, v29, s33, v214
	v_med3_f32 v30, v30, s33, v214
	v_mov_b32_e32 v29, v2
	v_lshlrev_b32_e32 v112, 16, v31
	v_and_b32_e32 v31, 0xffff0000, v31
	v_cvt_pk_fp8_f32 v29, v113, v30
	v_mul_f32_e32 v112, v180, v112
	v_mul_f32_e32 v31, v180, v31
	v_mul_f32_e32 v112, v112, v118
	v_mul_f32_e32 v31, v31, v119
	v_med3_f32 v112, v112, s33, v214
	v_med3_f32 v31, v31, s33, v214
	v_cvt_pk_fp8_f32 v29, v112, v31 op_sel:[0,0,1]
	v_mfma_f32_16x16x32_bf16 v[40:43], v[16:19], v[40:43], v[80:83]
	global_store_dwordx2 v[174:175], v[28:29], off offset:160
	ds_read_b128 v[28:31], v185 offset:192
	ds_read_b128 v[116:119], v185 offset:4544
	ds_read_b128 v[120:123], v185 offset:8896
	ds_read_b128 v[124:127], v185 offset:13248
	ds_read_b128 v[128:131], v185 offset:17600
	v_mfma_f32_16x16x32_bf16 v[80:83], v[16:19], v[132:135], v[84:87]
	v_lshlrev_b32_e32 v132, 16, v16
	v_mul_f32_e32 v132, v180, v132
	v_mfma_f32_16x16x32_bf16 v[84:87], v[16:19], v[136:139], v[88:91]
	v_mfma_f32_16x16x32_bf16 v[88:91], v[16:19], v[140:143], v[92:95]
	v_mfma_f32_16x16x32_bf16 v[92:95], v[16:19], v[144:147], v[96:99]
	s_nop 2
	ds_read_b128 v[96:99], v189 offset:768
	ds_read_b128 v[112:115], v189 offset:784
	v_and_b32_e32 v16, 0xffff0000, v16
	v_mul_f32_e32 v16, v180, v16
	s_waitcnt lgkmcnt(5)
	v_mfma_f32_16x16x32_bf16 v[116:119], v[4:7], v[116:119], v[80:83]
	s_waitcnt lgkmcnt(1)
; #define RT_WLOAD(W, c) do { const int cw_ = (c) < 16 ? (c) : 15; _Pragma("unroll") for (int i = 0; i < 3; ++i) { RT_TASK(i); W[i] = *(const GAS v4u*)(RW + (size_t)row * DM + cw_ * 128 + seg * 8); } } while (0)
; #define RT_WSTORE(W, c) do { _Pragma("unroll") for (int i = 0; i < 3; ++i) { RT_TASK(i); *(LAS v4u*)(wb + ((c) & 1) * WBUF + row * WROW + seg * 8) = W[i]; } } while (0)
; #define RT_XLOAD(XB, c) do { const int cc_ = (c) < 16 ? (c) : 15; _Pragma("unroll") for (int ks = 0; ks < 4; ++ks) XB[ks] = *(const GAS v4u*)(xrow + cc_ * 128 + 32 * ks); } while (0)
; #define RT_CHUNK(c, XB) do { const LAS bf16* cur = wb + ((c) & 1) * WBUF + c16 * WROW + 8 * g4; bf16x8 hA[5], hB[5]; RT_HLOAD(hA, 0); \
;         RT_HLOAD(hB, 1); RT_KSTEP(c, XB, 0, hA); RT_HLOAD(hA, 2); RT_KSTEP(c, XB, 1, hB); RT_HLOAD(hB, 3); RT_KSTEP(c, XB, 2, hA); RT_KSTEP(c, XB, 3, hB); } while (0)
; __device__ __forceinline__ void router_phase(const Ctx& C, const bf16* X, const float* rowss, const bf16* RW, const float* gain, const float* bg, const float* be, unsigned char* XN8, unsigned char* rt) {
;     ...
;     RT_WLOAD(wA, 0); RT_XLOAD(x0, 0); RT_XLOAD(x1, 1); RT_XLOAD(x2, 2); RT_WLOAD(wB, 1); RT_WSTORE(wA, 0);
;     __syncthreads();
; #pragma unroll 1
;     for (int c = 0; c < 16; c += 4) {
;         RT_WLOAD(wA, c + 2); RT_XLOAD(x3, c + 3); RT_CHUNK(c, x0); RT_WSTORE(wB, c + 1); __syncthreads();
;         RT_WLOAD(wB, c + 3); RT_XLOAD(x0, c + 4); RT_CHUNK(c + 1, x1); RT_WSTORE(wA, c + 2); __syncthreads();
;         RT_WLOAD(wA, c + 4); RT_XLOAD(x1, c + 5); RT_CHUNK(c + 2, x2); RT_WSTORE(wB, c + 3); __syncthreads();
;         RT_WLOAD(wB, c + 5); RT_XLOAD(x2, c + 6); RT_CHUNK(c + 3, x3); RT_WSTORE(wA, c + 4); __syncthreads();
	v_mul_f32_e32 v16, v16, v97
	v_lshlrev_b32_e32 v97, 16, v17
	v_mul_f32_e32 v96, v132, v96
	v_mul_f32_e32 v97, v180, v97
	v_mul_f32_e32 v97, v97, v98
	v_med3_f32 v96, v96, s33, v214
	v_med3_f32 v98, v16, s33, v214
	v_mov_b32_e32 v16, v2
	v_and_b32_e32 v17, 0xffff0000, v17
	v_cvt_pk_fp8_f32 v16, v96, v98
	v_mul_f32_e32 v17, v180, v17
	v_mul_f32_e32 v17, v17, v99
	v_med3_f32 v97, v97, s33, v214
	v_med3_f32 v17, v17, s33, v214
	v_cvt_pk_fp8_f32 v16, v97, v17 op_sel:[0,0,1]
	v_lshlrev_b32_e32 v17, 16, v18
	v_and_b32_e32 v18, 0xffff0000, v18
	v_mul_f32_e32 v17, v180, v17
	v_mul_f32_e32 v18, v180, v18
	s_waitcnt lgkmcnt(0)
	v_mul_f32_e32 v17, v17, v112
	v_mul_f32_e32 v18, v18, v113
	v_med3_f32 v97, v17, s33, v214
	v_med3_f32 v18, v18, s33, v214
	v_mov_b32_e32 v17, v2
	v_lshlrev_b32_e32 v96, 16, v19
	v_and_b32_e32 v19, 0xffff0000, v19
	v_cvt_pk_fp8_f32 v17, v97, v18
	v_mul_f32_e32 v96, v180, v96
	v_mul_f32_e32 v19, v180, v19
	v_mul_f32_e32 v96, v96, v114
	v_mul_f32_e32 v19, v19, v115
	v_med3_f32 v96, v96, s33, v214
	v_med3_f32 v19, v19, s33, v214
	v_cvt_pk_fp8_f32 v17, v96, v19 op_sel:[0,0,1]
	v_mfma_f32_16x16x32_bf16 v[112:115], v[4:7], v[28:31], v[40:43]
	global_store_dwordx2 v[174:175], v[16:17], off offset:192
	ds_read_b128 v[16:19], v189 offset:896
	ds_read_b128 v[28:31], v189 offset:912
	v_mfma_f32_16x16x32_bf16 v[120:123], v[4:7], v[120:123], v[84:87]
	v_lshlrev_b32_e32 v40, 16, v4
	v_mul_f32_e32 v40, v180, v40
	s_waitcnt lgkmcnt(1)
	v_mul_f32_e32 v16, v40, v16
	v_mfma_f32_16x16x32_bf16 v[124:127], v[4:7], v[124:127], v[88:91]
	v_med3_f32 v16, v16, s33, v214
	v_mfma_f32_16x16x32_bf16 v[128:131], v[4:7], v[128:131], v[92:95]
	v_and_b32_e32 v4, 0xffff0000, v4
	v_mul_f32_e32 v4, v180, v4
	v_mul_f32_e32 v4, v4, v17
	v_lshlrev_b32_e32 v17, 16, v5
	v_mul_f32_e32 v17, v180, v17
	v_mul_f32_e32 v17, v17, v18
	v_med3_f32 v18, v4, s33, v214
	v_mov_b32_e32 v4, v2
	v_and_b32_e32 v5, 0xffff0000, v5
	v_cvt_pk_fp8_f32 v4, v16, v18
	v_mul_f32_e32 v5, v180, v5
	v_mul_f32_e32 v5, v5, v19
	v_med3_f32 v17, v17, s33, v214
	v_med3_f32 v5, v5, s33, v214
	v_cvt_pk_fp8_f32 v4, v17, v5 op_sel:[0,0,1]
	v_lshlrev_b32_e32 v5, 16, v6
	v_and_b32_e32 v6, 0xffff0000, v6
	v_mul_f32_e32 v5, v180, v5
	v_mul_f32_e32 v6, v180, v6
	s_waitcnt lgkmcnt(0)
	v_mul_f32_e32 v5, v5, v28
	v_mul_f32_e32 v6, v6, v29
	v_med3_f32 v17, v5, s33, v214
	v_med3_f32 v6, v6, s33, v214
	v_mov_b32_e32 v5, v2
	v_lshlrev_b32_e32 v16, 16, v7
	v_and_b32_e32 v7, 0xffff0000, v7
	v_cvt_pk_fp8_f32 v5, v17, v6
	v_mul_f32_e32 v16, v180, v16
	v_mul_f32_e32 v7, v180, v7
	v_mul_f32_e32 v16, v16, v30
	v_mul_f32_e32 v7, v7, v31
	v_med3_f32 v16, v16, s33, v214
	v_med3_f32 v7, v7, s33, v214
	v_cvt_pk_fp8_f32 v5, v16, v7 op_sel:[0,0,1]
	global_store_dwordx2 v[174:175], v[4:5], off offset:224
	v_lshl_add_u64 v[4:5], s[12:13], 0, v[152:153]
	v_lshl_add_u64 v[4:5], v[4:5], 0, v[170:171]
	s_waitcnt vmcnt(21)
	ds_write_b128 v183, v[100:103] offset:24576
	s_waitcnt vmcnt(20)
	ds_write_b128 v181, v[104:107] offset:24576
	s_waitcnt vmcnt(19)
	ds_write_b128 v182, v[108:111] offset:24576
	s_waitcnt lgkmcnt(0)
	s_barrier
	global_load_dwordx4 v[100:103], v[4:5], off
	v_lshl_add_u64 v[4:5], s[12:13], 0, v[154:155]
	v_lshl_add_u64 v[4:5], v[4:5], 0, v[172:173]
	global_load_dwordx4 v[104:107], v[4:5], off
	v_lshl_add_u64 v[4:5], s[12:13], 0, v[156:157]
	v_lshl_add_u64 v[4:5], v[4:5], 0, v[172:173]
	global_load_dwordx4 v[108:111], v[4:5], off
	v_lshl_add_u64 v[4:5], v[158:159], 0, s[30:31]
	global_load_dwordx4 v[40:43], v[4:5], off offset:1280
	global_load_dwordx4 v[28:31], v[4:5], off offset:1344
	global_load_dwordx4 v[16:19], v[4:5], off offset:1408
	s_nop 0
	global_load_dwordx4 v[4:7], v[4:5], off offset:1472
	ds_read_b128 v[132:135], v184 offset:24576
	ds_read_b128 v[136:139], v184 offset:28928
	ds_read_b128 v[140:143], v184 offset:33280
	ds_read_b128 v[144:147], v184 offset:37632
	ds_read_b128 v[148:151], v184 offset:41984
	ds_read_b128 v[80:83], v184 offset:24640
	ds_read_b128 v[84:87], v184 offset:28992
	ds_read_b128 v[88:91], v184 offset:33344
	ds_read_b128 v[92:95], v184 offset:37696
	ds_read_b128 v[96:99], v184 offset:42048
	s_waitcnt lgkmcnt(9)
	v_mfma_f32_16x16x32_bf16 v[112:115], v[48:51], v[132:135], v[112:115]
	s_waitcnt lgkmcnt(8)
	v_mfma_f32_16x16x32_bf16 v[116:119], v[48:51], v[136:139], v[116:119]
	ds_read_b128 v[136:139], v189 offset:1024
	ds_read_b128 v[132:135], v189 offset:1040
	s_waitcnt lgkmcnt(9)
	v_mfma_f32_16x16x32_bf16 v[120:123], v[48:51], v[140:143], v[120:123]
	v_lshlrev_b32_e32 v140, 16, v48
	v_mul_f32_e32 v140, v180, v140
	s_waitcnt lgkmcnt(1)
	v_mul_f32_e32 v136, v140, v136
	v_mfma_f32_16x16x32_bf16 v[124:127], v[48:51], v[144:147], v[124:127]
	v_med3_f32 v136, v136, s33, v214
	v_mfma_f32_16x16x32_bf16 v[128:131], v[48:51], v[148:151], v[128:131]
	v_and_b32_e32 v48, 0xffff0000, v48
	v_mul_f32_e32 v48, v180, v48
	v_mul_f32_e32 v48, v48, v137
	v_lshlrev_b32_e32 v137, 16, v49
	v_mul_f32_e32 v137, v180, v137
	v_mul_f32_e32 v137, v137, v138
	v_med3_f32 v138, v48, s33, v214
	v_mov_b32_e32 v48, v2
	v_and_b32_e32 v49, 0xffff0000, v49
	v_cvt_pk_fp8_f32 v48, v136, v138
	v_mul_f32_e32 v49, v180, v49
	v_mul_f32_e32 v49, v49, v139
	v_med3_f32 v137, v137, s33, v214
	v_med3_f32 v49, v49, s33, v214
	v_cvt_pk_fp8_f32 v48, v137, v49 op_sel:[0,0,1]
	v_lshlrev_b32_e32 v49, 16, v50
	v_and_b32_e32 v50, 0xffff0000, v50
	v_mul_f32_e32 v49, v180, v49
	v_mul_f32_e32 v50, v180, v50
	s_waitcnt lgkmcnt(0)
; #define RT_WLOAD(W, c) do { const int cw_ = (c) < 16 ? (c) : 15; _Pragma("unroll") for (int i = 0; i < 3; ++i) { RT_TASK(i); W[i] = *(const GAS v4u*)(RW + (size_t)row * DM + cw_ * 128 + seg * 8); } } while (0)
; #define RT_WSTORE(W, c) do { _Pragma("unroll") for (int i = 0; i < 3; ++i) { RT_TASK(i); *(LAS v4u*)(wb + ((c) & 1) * WBUF + row * WROW + seg * 8) = W[i]; } } while (0)
; #define RT_XLOAD(XB, c) do { const int cc_ = (c) < 16 ? (c) : 15; _Pragma("unroll") for (int ks = 0; ks < 4; ++ks) XB[ks] = *(const GAS v4u*)(xrow + cc_ * 128 + 32 * ks); } while (0)
; #define RT_CHUNK(c, XB) do { const LAS bf16* cur = wb + ((c) & 1) * WBUF + c16 * WROW + 8 * g4; bf16x8 hA[5], hB[5]; RT_HLOAD(hA, 0); \
;         RT_HLOAD(hB, 1); RT_KSTEP(c, XB, 0, hA); RT_HLOAD(hA, 2); RT_KSTEP(c, XB, 1, hB); RT_HLOAD(hB, 3); RT_KSTEP(c, XB, 2, hA); RT_KSTEP(c, XB, 3, hB); } while (0)
; __device__ __forceinline__ void router_phase(const Ctx& C, const bf16* X, const float* rowss, const bf16* RW, const float* gain, const float* bg, const float* be, unsigned char* XN8, unsigned char* rt) {
;     ...
;     RT_WLOAD(wA, 0); RT_XLOAD(x0, 0); RT_XLOAD(x1, 1); RT_XLOAD(x2, 2); RT_WLOAD(wB, 1); RT_WSTORE(wA, 0);
;     __syncthreads();
; #pragma unroll 1
;     for (int c = 0; c < 16; c += 4) {
;         RT_WLOAD(wA, c + 2); RT_XLOAD(x3, c + 3); RT_CHUNK(c, x0); RT_WSTORE(wB, c + 1); __syncthreads();
;         RT_WLOAD(wB, c + 3); RT_XLOAD(x0, c + 4); RT_CHUNK(c + 1, x1); RT_WSTORE(wA, c + 2); __syncthreads();
;         RT_WLOAD(wA, c + 4); RT_XLOAD(x1, c + 5); RT_CHUNK(c + 2, x2); RT_WSTORE(wB, c + 3); __syncthreads();
;         RT_WLOAD(wB, c + 5); RT_XLOAD(x2, c + 6); RT_CHUNK(c + 3, x3); RT_WSTORE(wA, c + 4); __syncthreads();
	v_mul_f32_e32 v49, v49, v132
	v_mul_f32_e32 v50, v50, v133
	v_med3_f32 v133, v49, s33, v214
	v_med3_f32 v50, v50, s33, v214
	v_mov_b32_e32 v49, v2
	v_lshlrev_b32_e32 v132, 16, v51
	v_and_b32_e32 v51, 0xffff0000, v51
	v_cvt_pk_fp8_f32 v49, v133, v50
	v_mul_f32_e32 v132, v180, v132
	v_mul_f32_e32 v51, v180, v51
	v_mul_f32_e32 v132, v132, v134
	v_mul_f32_e32 v51, v51, v135
	v_med3_f32 v132, v132, s33, v214
	v_med3_f32 v51, v51, s33, v214
	v_cvt_pk_fp8_f32 v49, v132, v51 op_sel:[0,0,1]
	v_mfma_f32_16x16x32_bf16 v[80:83], v[36:39], v[80:83], v[112:115]
	global_store_dwordx2 v[174:175], v[48:49], off offset:256
	ds_read_b128 v[132:135], v184 offset:24704
	ds_read_b128 v[136:139], v184 offset:29056
	ds_read_b128 v[140:143], v184 offset:33408
	ds_read_b128 v[144:147], v184 offset:37760
	ds_read_b128 v[148:151], v184 offset:42112
	v_mfma_f32_16x16x32_bf16 v[112:115], v[36:39], v[88:91], v[120:123]
	ds_read_b128 v[48:51], v189 offset:1152
	ds_read_b128 v[88:91], v189 offset:1168
	v_mfma_f32_16x16x32_bf16 v[84:87], v[36:39], v[84:87], v[116:119]
	v_mfma_f32_16x16x32_bf16 v[116:119], v[36:39], v[92:95], v[124:127]
	v_lshlrev_b32_e32 v92, 16, v36
	v_mul_f32_e32 v92, v180, v92
	s_waitcnt lgkmcnt(1)
	v_mul_f32_e32 v48, v92, v48
	v_mfma_f32_16x16x32_bf16 v[120:123], v[36:39], v[96:99], v[128:131]
	v_and_b32_e32 v36, 0xffff0000, v36
	v_mul_f32_e32 v36, v180, v36
	v_mul_f32_e32 v36, v36, v49
	v_lshlrev_b32_e32 v49, 16, v37
	v_mul_f32_e32 v49, v180, v49
	v_mul_f32_e32 v49, v49, v50
	v_med3_f32 v48, v48, s33, v214
	v_med3_f32 v50, v36, s33, v214
	v_mov_b32_e32 v36, v2
	v_and_b32_e32 v37, 0xffff0000, v37
	v_cvt_pk_fp8_f32 v36, v48, v50
	v_mul_f32_e32 v37, v180, v37
	v_mul_f32_e32 v37, v37, v51
	v_med3_f32 v49, v49, s33, v214
	v_med3_f32 v37, v37, s33, v214
	v_cvt_pk_fp8_f32 v36, v49, v37 op_sel:[0,0,1]
	v_lshlrev_b32_e32 v37, 16, v38
	v_and_b32_e32 v38, 0xffff0000, v38
	v_mul_f32_e32 v37, v180, v37
	v_mul_f32_e32 v38, v180, v38
	s_waitcnt lgkmcnt(0)
	v_mul_f32_e32 v37, v37, v88
	v_mul_f32_e32 v38, v38, v89
	v_med3_f32 v49, v37, s33, v214
	v_med3_f32 v38, v38, s33, v214
	v_mov_b32_e32 v37, v2
	v_lshlrev_b32_e32 v48, 16, v39
	v_and_b32_e32 v39, 0xffff0000, v39
	v_cvt_pk_fp8_f32 v37, v49, v38
	v_mul_f32_e32 v48, v180, v48
	v_mul_f32_e32 v39, v180, v39
	v_mul_f32_e32 v48, v48, v90
	v_mul_f32_e32 v39, v39, v91
	v_med3_f32 v48, v48, s33, v214
	v_med3_f32 v39, v39, s33, v214
	v_cvt_pk_fp8_f32 v37, v48, v39 op_sel:[0,0,1]
	v_mfma_f32_16x16x32_bf16 v[80:83], v[20:23], v[132:135], v[80:83]
	v_lshlrev_b32_e32 v132, 16, v20
	v_mul_f32_e32 v132, v180, v132
	global_store_dwordx2 v[174:175], v[36:37], off offset:288
	ds_read_b128 v[36:39], v184 offset:24768
	ds_read_b128 v[48:51], v184 offset:29120
	ds_read_b128 v[88:91], v184 offset:33472
	ds_read_b128 v[92:95], v184 offset:37824
	ds_read_b128 v[96:99], v184 offset:42176
	ds_read_b128 v[128:131], v189 offset:1280
	ds_read_b128 v[124:127], v189 offset:1296
	v_mfma_f32_16x16x32_bf16 v[84:87], v[20:23], v[136:139], v[84:87]
	s_waitcnt lgkmcnt(1)
	v_mul_f32_e32 v128, v132, v128
	v_mfma_f32_16x16x32_bf16 v[112:115], v[20:23], v[140:143], v[112:115]
	v_med3_f32 v128, v128, s33, v214
	v_mfma_f32_16x16x32_bf16 v[116:119], v[20:23], v[144:147], v[116:119]
	v_mfma_f32_16x16x32_bf16 v[120:123], v[20:23], v[148:151], v[120:123]
	v_and_b32_e32 v20, 0xffff0000, v20
	v_mul_f32_e32 v20, v180, v20
	v_mul_f32_e32 v20, v20, v129
	v_lshlrev_b32_e32 v129, 16, v21
	v_mul_f32_e32 v129, v180, v129
	v_mul_f32_e32 v129, v129, v130
	v_med3_f32 v130, v20, s33, v214
	v_mov_b32_e32 v20, v2
	v_and_b32_e32 v21, 0xffff0000, v21
	v_cvt_pk_fp8_f32 v20, v128, v130
	v_mul_f32_e32 v21, v180, v21
	v_mul_f32_e32 v21, v21, v131
	v_med3_f32 v129, v129, s33, v214
	v_med3_f32 v21, v21, s33, v214
	v_cvt_pk_fp8_f32 v20, v129, v21 op_sel:[0,0,1]
	v_lshlrev_b32_e32 v21, 16, v22
	v_and_b32_e32 v22, 0xffff0000, v22
	v_mul_f32_e32 v21, v180, v21
	v_mul_f32_e32 v22, v180, v22
	s_waitcnt lgkmcnt(0)
	v_mul_f32_e32 v21, v21, v124
	v_mul_f32_e32 v22, v22, v125
	v_med3_f32 v125, v21, s33, v214
	v_med3_f32 v22, v22, s33, v214
	v_mov_b32_e32 v21, v2
	v_lshlrev_b32_e32 v124, 16, v23
	v_and_b32_e32 v23, 0xffff0000, v23
	v_cvt_pk_fp8_f32 v21, v125, v22
	v_mul_f32_e32 v124, v180, v124
	v_mul_f32_e32 v23, v180, v23
	v_mul_f32_e32 v124, v124, v126
	v_mul_f32_e32 v23, v23, v127
	v_med3_f32 v124, v124, s33, v214
	v_med3_f32 v23, v23, s33, v214
	v_cvt_pk_fp8_f32 v21, v124, v23 op_sel:[0,0,1]
	v_mfma_f32_16x16x32_bf16 v[80:83], v[8:11], v[36:39], v[80:83]
	global_store_dwordx2 v[174:175], v[20:21], off offset:320
	ds_read_b128 v[36:39], v189 offset:1408
	ds_read_b128 v[20:23], v189 offset:1424
	v_mfma_f32_16x16x32_bf16 v[84:87], v[8:11], v[48:51], v[84:87]
	v_lshlrev_b32_e32 v48, 16, v8
	v_mul_f32_e32 v48, v180, v48
	s_waitcnt lgkmcnt(1)
	v_mul_f32_e32 v36, v48, v36
	v_mfma_f32_16x16x32_bf16 v[88:91], v[8:11], v[88:91], v[112:115]
	v_med3_f32 v36, v36, s33, v214
	v_mfma_f32_16x16x32_bf16 v[92:95], v[8:11], v[92:95], v[116:119]
	v_mfma_f32_16x16x32_bf16 v[96:99], v[8:11], v[96:99], v[120:123]
	v_and_b32_e32 v8, 0xffff0000, v8
	v_mul_f32_e32 v8, v180, v8
	v_mul_f32_e32 v8, v8, v37
	v_lshlrev_b32_e32 v37, 16, v9
	v_mul_f32_e32 v37, v180, v37
	v_mul_f32_e32 v37, v37, v38
	v_med3_f32 v38, v8, s33, v214
	v_mov_b32_e32 v8, v2
	v_and_b32_e32 v9, 0xffff0000, v9
	v_cvt_pk_fp8_f32 v8, v36, v38
	v_mul_f32_e32 v9, v180, v9
	v_mul_f32_e32 v9, v9, v39
	v_med3_f32 v37, v37, s33, v214
	v_med3_f32 v9, v9, s33, v214
	v_cvt_pk_fp8_f32 v8, v37, v9 op_sel:[0,0,1]
	v_lshlrev_b32_e32 v9, 16, v10
	v_and_b32_e32 v10, 0xffff0000, v10
	v_mul_f32_e32 v9, v180, v9
	v_mul_f32_e32 v10, v180, v10
	s_waitcnt lgkmcnt(0)
	v_mul_f32_e32 v9, v9, v20
	v_mul_f32_e32 v10, v10, v21
	v_med3_f32 v21, v9, s33, v214
	v_med3_f32 v10, v10, s33, v214
	v_mov_b32_e32 v9, v2
	v_lshlrev_b32_e32 v20, 16, v11
	v_and_b32_e32 v11, 0xffff0000, v11
	v_cvt_pk_fp8_f32 v9, v21, v10
	v_mul_f32_e32 v20, v180, v20
	v_mul_f32_e32 v11, v180, v11
	v_mul_f32_e32 v20, v20, v22
	v_mul_f32_e32 v11, v11, v23
	v_med3_f32 v20, v20, s33, v214
	v_med3_f32 v11, v11, s33, v214
	v_cvt_pk_fp8_f32 v9, v20, v11 op_sel:[0,0,1]
	global_store_dwordx2 v[174:175], v[8:9], off offset:352
	v_lshl_add_u64 v[8:9], s[10:11], 0, v[152:153]
	v_lshl_add_u64 v[8:9], v[8:9], 0, v[170:171]
	s_waitcnt vmcnt(21)
	ds_write_b128 v186, v[52:55]
	s_waitcnt vmcnt(20)
	ds_write_b128 v187, v[56:59]
	s_waitcnt vmcnt(19)
	ds_write_b128 v188, v[60:63]
	s_waitcnt lgkmcnt(0)
	s_barrier
; #define RT_WLOAD(W, c) do { const int cw_ = (c) < 16 ? (c) : 15; _Pragma("unroll") for (int i = 0; i < 3; ++i) { RT_TASK(i); W[i] = *(const GAS v4u*)(RW + (size_t)row * DM + cw_ * 128 + seg * 8); } } while (0)
; #define RT_WSTORE(W, c) do { _Pragma("unroll") for (int i = 0; i < 3; ++i) { RT_TASK(i); *(LAS v4u*)(wb + ((c) & 1) * WBUF + row * WROW + seg * 8) = W[i]; } } while (0)
; #define RT_XLOAD(XB, c) do { const int cc_ = (c) < 16 ? (c) : 15; _Pragma("unroll") for (int ks = 0; ks < 4; ++ks) XB[ks] = *(const GAS v4u*)(xrow + cc_ * 128 + 32 * ks); } while (0)
; #define RT_CHUNK(c, XB) do { const LAS bf16* cur = wb + ((c) & 1) * WBUF + c16 * WROW + 8 * g4; bf16x8 hA[5], hB[5]; RT_HLOAD(hA, 0); \
;         RT_HLOAD(hB, 1); RT_KSTEP(c, XB, 0, hA); RT_HLOAD(hA, 2); RT_KSTEP(c, XB, 1, hB); RT_HLOAD(hB, 3); RT_KSTEP(c, XB, 2, hA); RT_KSTEP(c, XB, 3, hB); } while (0)
; __device__ __forceinline__ void router_phase(const Ctx& C, const bf16* X, const float* rowss, const bf16* RW, const float* gain, const float* bg, const float* be, unsigned char* XN8, unsigned char* rt) {
;     ...
;     RT_WLOAD(wA, 0); RT_XLOAD(x0, 0); RT_XLOAD(x1, 1); RT_XLOAD(x2, 2); RT_WLOAD(wB, 1); RT_WSTORE(wA, 0);
;     __syncthreads();
; #pragma unroll 1
;     for (int c = 0; c < 16; c += 4) {
;         RT_WLOAD(wA, c + 2); RT_XLOAD(x3, c + 3); RT_CHUNK(c, x0); RT_WSTORE(wB, c + 1); __syncthreads();
;         RT_WLOAD(wB, c + 3); RT_XLOAD(x0, c + 4); RT_CHUNK(c + 1, x1); RT_WSTORE(wA, c + 2); __syncthreads();
;         RT_WLOAD(wA, c + 4); RT_XLOAD(x1, c + 5); RT_CHUNK(c + 2, x2); RT_WSTORE(wB, c + 3); __syncthreads();
;         RT_WLOAD(wB, c + 5); RT_XLOAD(x2, c + 6); RT_CHUNK(c + 3, x3); RT_WSTORE(wA, c + 4); __syncthreads();
	global_load_dwordx4 v[60:63], v[8:9], off offset:1280
	v_lshl_add_u64 v[8:9], s[10:11], 0, v[154:155]
	v_lshl_add_u64 v[8:9], v[8:9], 0, v[172:173]
	global_load_dwordx4 v[56:59], v[8:9], off offset:1280
	v_lshl_add_u64 v[8:9], s[10:11], 0, v[156:157]
	v_lshl_add_u64 v[8:9], v[8:9], 0, v[172:173]
	global_load_dwordx4 v[52:55], v[8:9], off offset:1280
	v_lshl_add_u64 v[8:9], v[158:159], 0, s[8:9]
	global_load_dwordx4 v[48:51], v[8:9], off offset:1536
	global_load_dwordx4 v[36:39], v[8:9], off offset:1600
	global_load_dwordx4 v[20:23], v[8:9], off offset:1664
	s_nop 0
	global_load_dwordx4 v[8:11], v[8:9], off offset:1728
	ds_read_b128 v[132:135], v185
	ds_read_b128 v[136:139], v185 offset:4352
	ds_read_b128 v[140:143], v185 offset:8704
	ds_read_b128 v[144:147], v185 offset:13056
	ds_read_b128 v[148:151], v185 offset:17408
	ds_read_b128 v[112:115], v185 offset:64
	ds_read_b128 v[116:119], v185 offset:4416
	ds_read_b128 v[120:123], v185 offset:8768
	ds_read_b128 v[124:127], v185 offset:13120
	ds_read_b128 v[128:131], v185 offset:17472
	s_waitcnt lgkmcnt(9)
	v_mfma_f32_16x16x32_bf16 v[80:83], v[76:79], v[132:135], v[80:83]
	s_mov_b64 s[8:9], 0x200
	v_lshl_add_u64 v[160:161], v[160:161], 0, s[8:9]
	s_mov_b32 s9, s17
	s_waitcnt lgkmcnt(8)
	v_mfma_f32_16x16x32_bf16 v[84:87], v[76:79], v[136:139], v[84:87]
	ds_read_b128 v[132:135], v189 offset:1536
	ds_read_b128 v[136:139], v189 offset:1552
	s_waitcnt lgkmcnt(9)
	v_mfma_f32_16x16x32_bf16 v[88:91], v[76:79], v[140:143], v[88:91]
	v_lshlrev_b32_e32 v140, 16, v76
	v_mul_f32_e32 v140, v180, v140
	s_waitcnt lgkmcnt(1)
	v_mul_f32_e32 v132, v140, v132
	v_mfma_f32_16x16x32_bf16 v[92:95], v[76:79], v[144:147], v[92:95]
	v_med3_f32 v132, v132, s33, v214
	v_mfma_f32_16x16x32_bf16 v[96:99], v[76:79], v[148:151], v[96:99]
	v_and_b32_e32 v76, 0xffff0000, v76
	v_mul_f32_e32 v76, v180, v76
	v_mul_f32_e32 v76, v76, v133
	v_lshlrev_b32_e32 v133, 16, v77
	v_mul_f32_e32 v133, v180, v133
	v_mul_f32_e32 v133, v133, v134
	v_med3_f32 v134, v76, s33, v214
	v_mov_b32_e32 v76, v2
	v_and_b32_e32 v77, 0xffff0000, v77
	v_cvt_pk_fp8_f32 v76, v132, v134
	v_mul_f32_e32 v77, v180, v77
	v_mul_f32_e32 v77, v77, v135
	v_med3_f32 v133, v133, s33, v214
	v_med3_f32 v77, v77, s33, v214
	v_cvt_pk_fp8_f32 v76, v133, v77 op_sel:[0,0,1]
	v_lshlrev_b32_e32 v77, 16, v78
	v_and_b32_e32 v78, 0xffff0000, v78
	v_mul_f32_e32 v77, v180, v77
	v_mul_f32_e32 v78, v180, v78
	s_waitcnt lgkmcnt(0)
	v_mul_f32_e32 v77, v77, v136
	v_mul_f32_e32 v78, v78, v137
	v_med3_f32 v133, v77, s33, v214
	v_med3_f32 v78, v78, s33, v214
	v_mov_b32_e32 v77, v2
	v_lshlrev_b32_e32 v132, 16, v79
	v_and_b32_e32 v79, 0xffff0000, v79
	v_cvt_pk_fp8_f32 v77, v133, v78
	v_mul_f32_e32 v132, v180, v132
	v_mul_f32_e32 v79, v180, v79
	v_mul_f32_e32 v132, v132, v138
	v_mul_f32_e32 v79, v79, v139
	v_med3_f32 v132, v132, s33, v214
	v_med3_f32 v79, v79, s33, v214
	v_cvt_pk_fp8_f32 v77, v132, v79 op_sel:[0,0,1]
	v_mfma_f32_16x16x32_bf16 v[80:83], v[72:75], v[112:115], v[80:83]
	global_store_dwordx2 v[174:175], v[76:77], off offset:384
	ds_read_b128 v[76:79], v185 offset:128
	ds_read_b128 v[132:135], v185 offset:4480
	ds_read_b128 v[136:139], v185 offset:8832
	ds_read_b128 v[140:143], v185 offset:13184
	ds_read_b128 v[144:147], v185 offset:17536
	v_mfma_f32_16x16x32_bf16 v[84:87], v[72:75], v[116:119], v[84:87]
	ds_read_b128 v[112:115], v189 offset:1664
	ds_read_b128 v[116:119], v189 offset:1680
	v_mfma_f32_16x16x32_bf16 v[88:91], v[72:75], v[120:123], v[88:91]
	v_lshlrev_b32_e32 v120, 16, v72
	v_mul_f32_e32 v120, v180, v120
	s_waitcnt lgkmcnt(1)
	v_mul_f32_e32 v112, v120, v112
	v_mfma_f32_16x16x32_bf16 v[92:95], v[72:75], v[124:127], v[92:95]
	v_med3_f32 v112, v112, s33, v214
	v_mfma_f32_16x16x32_bf16 v[96:99], v[72:75], v[128:131], v[96:99]
	v_and_b32_e32 v72, 0xffff0000, v72
	v_mul_f32_e32 v72, v180, v72
	v_mul_f32_e32 v72, v72, v113
	v_lshlrev_b32_e32 v113, 16, v73
	v_mul_f32_e32 v113, v180, v113
	v_mul_f32_e32 v113, v113, v114
	v_med3_f32 v114, v72, s33, v214
	v_mov_b32_e32 v72, v2
	v_and_b32_e32 v73, 0xffff0000, v73
	v_cvt_pk_fp8_f32 v72, v112, v114
	v_mul_f32_e32 v73, v180, v73
	v_mul_f32_e32 v73, v73, v115
	v_med3_f32 v113, v113, s33, v214
	v_med3_f32 v73, v73, s33, v214
	v_cvt_pk_fp8_f32 v72, v113, v73 op_sel:[0,0,1]
	v_lshlrev_b32_e32 v73, 16, v74
	v_and_b32_e32 v74, 0xffff0000, v74
	v_mul_f32_e32 v73, v180, v73
	v_mul_f32_e32 v74, v180, v74
	s_waitcnt lgkmcnt(0)
	v_mul_f32_e32 v73, v73, v116
	v_mul_f32_e32 v74, v74, v117
	v_med3_f32 v113, v73, s33, v214
	v_med3_f32 v74, v74, s33, v214
	v_mov_b32_e32 v73, v2
	v_lshlrev_b32_e32 v112, 16, v75
	v_and_b32_e32 v75, 0xffff0000, v75
	v_cvt_pk_fp8_f32 v73, v113, v74
	v_mul_f32_e32 v112, v180, v112
	v_mul_f32_e32 v75, v180, v75
	v_mul_f32_e32 v112, v112, v118
	v_mul_f32_e32 v75, v75, v119
	v_med3_f32 v112, v112, s33, v214
	v_med3_f32 v75, v75, s33, v214
	v_cvt_pk_fp8_f32 v73, v112, v75 op_sel:[0,0,1]
	v_mfma_f32_16x16x32_bf16 v[76:79], v[68:71], v[76:79], v[80:83]
	global_store_dwordx2 v[174:175], v[72:73], off offset:416
	ds_read_b128 v[72:75], v185 offset:192
	ds_read_b128 v[112:115], v185 offset:4544
	ds_read_b128 v[116:119], v185 offset:8896
	ds_read_b128 v[120:123], v185 offset:13248
	ds_read_b128 v[124:127], v185 offset:17600
	v_mfma_f32_16x16x32_bf16 v[128:131], v[68:71], v[140:143], v[92:95]
	ds_read_b128 v[80:83], v189 offset:1792
	s_nop 1
	ds_read_b128 v[92:95], v189 offset:1808
	v_mfma_f32_16x16x32_bf16 v[84:87], v[68:71], v[132:135], v[84:87]
	v_mfma_f32_16x16x32_bf16 v[88:91], v[68:71], v[136:139], v[88:91]
	v_mfma_f32_16x16x32_bf16 v[132:135], v[68:71], v[144:147], v[96:99]
	s_nop 2
	v_lshlrev_b32_e32 v96, 16, v68
	v_and_b32_e32 v68, 0xffff0000, v68
	v_mul_f32_e32 v68, v180, v68
	v_mul_f32_e32 v96, v180, v96
	s_waitcnt lgkmcnt(1)
; #define RT_WLOAD(W, c) do { const int cw_ = (c) < 16 ? (c) : 15; _Pragma("unroll") for (int i = 0; i < 3; ++i) { RT_TASK(i); W[i] = *(const GAS v4u*)(RW + (size_t)row * DM + cw_ * 128 + seg * 8); } } while (0)
; #define RT_WSTORE(W, c) do { _Pragma("unroll") for (int i = 0; i < 3; ++i) { RT_TASK(i); *(LAS v4u*)(wb + ((c) & 1) * WBUF + row * WROW + seg * 8) = W[i]; } } while (0)
; #define RT_XLOAD(XB, c) do { const int cc_ = (c) < 16 ? (c) : 15; _Pragma("unroll") for (int ks = 0; ks < 4; ++ks) XB[ks] = *(const GAS v4u*)(xrow + cc_ * 128 + 32 * ks); } while (0)
; #define RT_CHUNK(c, XB) do { const LAS bf16* cur = wb + ((c) & 1) * WBUF + c16 * WROW + 8 * g4; bf16x8 hA[5], hB[5]; RT_HLOAD(hA, 0); \
;         RT_HLOAD(hB, 1); RT_KSTEP(c, XB, 0, hA); RT_HLOAD(hA, 2); RT_KSTEP(c, XB, 1, hB); RT_HLOAD(hB, 3); RT_KSTEP(c, XB, 2, hA); RT_KSTEP(c, XB, 3, hB); } while (0)
; __device__ __forceinline__ void router_phase(const Ctx& C, const bf16* X, const float* rowss, const bf16* RW, const float* gain, const float* bg, const float* be, unsigned char* XN8, unsigned char* rt) {
;     ...
;     RT_WLOAD(wA, 0); RT_XLOAD(x0, 0); RT_XLOAD(x1, 1); RT_XLOAD(x2, 2); RT_WLOAD(wB, 1); RT_WSTORE(wA, 0);
;     __syncthreads();
; #pragma unroll 1
;     for (int c = 0; c < 16; c += 4) {
;         RT_WLOAD(wA, c + 2); RT_XLOAD(x3, c + 3); RT_CHUNK(c, x0); RT_WSTORE(wB, c + 1); __syncthreads();
;         RT_WLOAD(wB, c + 3); RT_XLOAD(x0, c + 4); RT_CHUNK(c + 1, x1); RT_WSTORE(wA, c + 2); __syncthreads();
;         RT_WLOAD(wA, c + 4); RT_XLOAD(x1, c + 5); RT_CHUNK(c + 2, x2); RT_WSTORE(wB, c + 3); __syncthreads();
;         RT_WLOAD(wB, c + 5); RT_XLOAD(x2, c + 6); RT_CHUNK(c + 3, x3); RT_WSTORE(wA, c + 4); __syncthreads();
;     ...
;     float rs4[4];
; #pragma unroll
;     for (int r = 0; r < 4; ++r) rs4[r] = __shfl(rstd_l, ((4 * g4 + r) & 7) * 8);
;     if (g4 < 2) {
; #pragma unroll
;         for (int r = 0; r < 4; ++r) { const int row = 4 * g4 + r;
; #pragma unroll
;             for (int nt = 0; nt < 5; ++nt) { const int o = 16 * nt + c16; if (o < 72) lg[row * 80 + o] = acc[nt][r] * rs4[r] + (o < 8 ? bg[o] : be[o - 8]); } }
;     }
	v_mul_f32_e32 v68, v68, v81
	v_lshlrev_b32_e32 v81, 16, v69
	v_mul_f32_e32 v80, v96, v80
	v_mul_f32_e32 v81, v180, v81
	v_mul_f32_e32 v81, v81, v82
	v_med3_f32 v80, v80, s33, v214
	v_med3_f32 v82, v68, s33, v214
	v_mov_b32_e32 v68, v2
	v_and_b32_e32 v69, 0xffff0000, v69
	v_cvt_pk_fp8_f32 v68, v80, v82
	v_mul_f32_e32 v69, v180, v69
	v_mul_f32_e32 v69, v69, v83
	v_med3_f32 v81, v81, s33, v214
	v_med3_f32 v69, v69, s33, v214
	v_cvt_pk_fp8_f32 v68, v81, v69 op_sel:[0,0,1]
	v_lshlrev_b32_e32 v69, 16, v70
	v_and_b32_e32 v70, 0xffff0000, v70
	v_mul_f32_e32 v69, v180, v69
	v_mul_f32_e32 v70, v180, v70
	s_waitcnt lgkmcnt(0)
	v_mul_f32_e32 v69, v69, v92
	v_mul_f32_e32 v70, v70, v93
	v_med3_f32 v81, v69, s33, v214
	v_med3_f32 v70, v70, s33, v214
	v_mov_b32_e32 v69, v2
	v_lshlrev_b32_e32 v80, 16, v71
	v_and_b32_e32 v71, 0xffff0000, v71
	v_cvt_pk_fp8_f32 v69, v81, v70
	v_mul_f32_e32 v80, v180, v80
	v_mul_f32_e32 v71, v180, v71
	v_mul_f32_e32 v80, v80, v94
	v_mul_f32_e32 v71, v71, v95
	v_med3_f32 v80, v80, s33, v214
	v_med3_f32 v71, v71, s33, v214
	v_cvt_pk_fp8_f32 v69, v80, v71 op_sel:[0,0,1]
	v_mfma_f32_16x16x32_bf16 v[80:83], v[64:67], v[72:75], v[76:79]
	global_store_dwordx2 v[174:175], v[68:69], off offset:448
	ds_read_b128 v[68:71], v189 offset:1920
	ds_read_b128 v[72:75], v189 offset:1936
	v_mfma_f32_16x16x32_bf16 v[92:95], v[64:67], v[112:115], v[84:87]
	v_lshlrev_b32_e32 v76, 16, v64
	v_mul_f32_e32 v76, v180, v76
	s_waitcnt lgkmcnt(1)
	v_mul_f32_e32 v68, v76, v68
	v_mfma_f32_16x16x32_bf16 v[88:91], v[64:67], v[116:119], v[88:91]
	v_med3_f32 v68, v68, s33, v214
	v_add_u32_e32 v189, 0x800, v189
	v_mfma_f32_16x16x32_bf16 v[96:99], v[64:67], v[120:123], v[128:131]
	v_mfma_f32_16x16x32_bf16 v[84:87], v[64:67], v[124:127], v[132:135]
	v_and_b32_e32 v64, 0xffff0000, v64
	v_mul_f32_e32 v64, v180, v64
	v_mul_f32_e32 v64, v64, v69
	v_lshlrev_b32_e32 v69, 16, v65
	v_mul_f32_e32 v69, v180, v69
	v_mul_f32_e32 v69, v69, v70
	v_med3_f32 v70, v64, s33, v214
	v_mov_b32_e32 v64, v2
	v_and_b32_e32 v65, 0xffff0000, v65
	v_cvt_pk_fp8_f32 v64, v68, v70
	v_mul_f32_e32 v65, v180, v65
	v_mul_f32_e32 v65, v65, v71
	v_med3_f32 v69, v69, s33, v214
	v_med3_f32 v65, v65, s33, v214
	v_cvt_pk_fp8_f32 v64, v69, v65 op_sel:[0,0,1]
	v_lshlrev_b32_e32 v65, 16, v66
	v_and_b32_e32 v66, 0xffff0000, v66
	v_mul_f32_e32 v65, v180, v65
	v_mul_f32_e32 v66, v180, v66
	s_waitcnt lgkmcnt(0)
	v_mul_f32_e32 v65, v65, v72
	v_mul_f32_e32 v66, v66, v73
	v_med3_f32 v69, v65, s33, v214
	v_med3_f32 v66, v66, s33, v214
	v_mov_b32_e32 v65, v2
	v_lshlrev_b32_e32 v68, 16, v67
	v_and_b32_e32 v67, 0xffff0000, v67
	v_cvt_pk_fp8_f32 v65, v69, v66
	v_mul_f32_e32 v68, v180, v68
	v_mul_f32_e32 v67, v180, v67
	v_mul_f32_e32 v68, v68, v74
	v_mul_f32_e32 v67, v67, v75
	v_med3_f32 v68, v68, s33, v214
	v_med3_f32 v67, v67, s33, v214
	v_cvt_pk_fp8_f32 v65, v68, v67 op_sel:[0,0,1]
	global_store_dwordx2 v[174:175], v[64:65], off offset:480
	s_waitcnt vmcnt(21)
	ds_write_b128 v183, v[100:103] offset:24576
	s_waitcnt vmcnt(20)
	ds_write_b128 v181, v[104:107] offset:24576
	s_waitcnt vmcnt(19)
	ds_write_b128 v182, v[108:111] offset:24576
	s_waitcnt lgkmcnt(0)
	s_barrier
	s_cbranch_scc0 .LBB0_986
	s_waitcnt vmcnt(15)
	v_lshlrev_b32_e32 v4, 7, v179
	s_movk_i32 s2, 0x80
	v_and_or_b32 v4, v4, s2, v178
	s_waitcnt vmcnt(4)
	ds_bpermute_b32 v10, v4, v177
	ds_bpermute_b32 v8, v4, v177 offset:32
	ds_bpermute_b32 v7, v4, v177 offset:64
	ds_bpermute_b32 v6, v4, v177 offset:96
	v_cmp_gt_i32_e32 vcc, 2, v179
	s_and_saveexec_b64 s[2:3], vcc
	s_cbranch_execz .LBB0_996
	v_readlane_b32 s8, v254, 20
	s_lshl_b32 s30, s8, 3
	v_readlane_b32 s9, v254, 21
	s_lshl_b32 s8, s8, 6
	s_lshl_b64 s[10:11], s[30:31], 2
	s_mov_b32 s9, s31
	s_add_u32 s6, s6, s10
	s_addc_u32 s7, s7, s11
	s_lshl_b64 s[8:9], s[8:9], 2
	s_add_u32 s4, s4, s8
	v_lshlrev_b32_e32 v14, 2, v1
	v_mov_b32_e32 v15, v2
	s_addc_u32 s5, s5, s9
	v_lshl_add_u64 v[12:13], s[6:7], 0, v[14:15]
	s_movk_i32 s6, 0xffe0
	v_lshl_add_u64 v[4:5], s[4:5], 0, v[14:15]
	s_mov_b32 s7, -1
	v_cmp_gt_u32_e32 vcc, 8, v1
	v_lshl_add_u64 v[16:17], v[4:5], 0, s[6:7]
	s_movk_i32 s8, 0x500
	v_cndmask_b32_e32 v13, v17, v13, vcc
	v_cndmask_b32_e32 v12, v16, v12, vcc
	global_load_dword v11, v[12:13], off
	v_mul_lo_u32 v9, v179, s8
	global_load_dword v12, v14, s[4:5] offset:32
	global_load_dword v220, v14, s[4:5] offset:96
	global_load_dword v221, v14, s[4:5] offset:160
	v_readlane_b32 s6, v253, 61
	v_or_b32_e32 v1, 64, v1
	s_waitcnt vmcnt(3) lgkmcnt(3)
	v_fma_f32 v13, v80, v10, v11
	v_add3_u32 v9, s6, v9, v14
	s_waitcnt vmcnt(2)
	v_fma_f32 v16, v92, v10, v12
	v_add_u32_e32 v15, 0x400, v9
	ds_write2_b32 v15, v13, v16 offset1:16
	s_waitcnt vmcnt(1)
	v_fma_f32 v16, v88, v10, v220
	s_movk_i32 s4, 0x48
	v_cmp_gt_u32_e32 vcc, s4, v1
	s_waitcnt vmcnt(0)
	v_fma_f32 v17, v96, v10, v221
	ds_write2_b32 v15, v16, v17 offset0:32 offset1:48
	s_and_saveexec_b64 s[4:5], vcc
	s_cbranch_execz .LBB0_990
	global_load_dword v222, v[4:5], off offset:224
	s_waitcnt vmcnt(0)
	v_fma_f32 v1, v84, v10, v222
	ds_write_b32 v9, v1 offset:1280
.LBB0_990:
	s_or_b64 exec, exec, s[4:5]
	s_waitcnt lgkmcnt(4)
	v_fma_f32 v1, v81, v8, v11
	v_fma_f32 v10, v93, v8, v12
	ds_write2_b32 v15, v1, v10 offset0:80 offset1:96
	v_fma_f32 v1, v89, v8, v220
	v_fma_f32 v10, v97, v8, v221
	ds_write2_b32 v15, v1, v10 offset0:112 offset1:128
	s_and_saveexec_b64 s[4:5], vcc
	s_cbranch_execz .LBB0_992
	v_fma_f32 v1, v85, v8, v222
	ds_write_b32 v9, v1 offset:1600
.LBB0_992:
	s_or_b64 exec, exec, s[4:5]
	s_waitcnt lgkmcnt(5)
	v_fma_f32 v1, v82, v7, v11
	v_fma_f32 v8, v94, v7, v12
	ds_write2_b32 v15, v1, v8 offset0:160 offset1:176
	v_fma_f32 v1, v90, v7, v220
	v_fma_f32 v8, v98, v7, v221
	ds_write2_b32 v15, v1, v8 offset0:192 offset1:208
	s_and_saveexec_b64 s[4:5], vcc
	s_cbranch_execz .LBB0_994
	v_fma_f32 v1, v86, v7, v222
	ds_write_b32 v9, v1 offset:1920
.LBB0_994:
	s_or_b64 exec, exec, s[4:5]
	s_waitcnt lgkmcnt(6)
	v_fmac_f32_e32 v11, v83, v6
	v_fmac_f32_e32 v12, v95, v6
	v_add_u32_e32 v1, 0x600, v9
	ds_write2_b32 v1, v11, v12 offset0:112 offset1:128
	v_fmac_f32_e32 v220, v91, v6
	v_fmac_f32_e32 v221, v99, v6
	v_add_u32_e32 v1, 0x800, v9
	ds_write2_b32 v1, v220, v221 offset0:16 offset1:32
	s_and_b64 exec, exec, vcc
	s_cbranch_execz .LBB0_996
	v_fma_f32 v1, v87, v6, v222
	ds_write_b32 v9, v1 offset:2240
